# speedup vs baseline: 1.0852x; 1.0070x over previous
_Z11attn_kernelPKDF16_S0_S0_PDF16_P15HIP_vector_typeIfLj2EE:
	s_mov_b32 s28, s2
	s_load_dwordx4 s[32:35], s[0:1], 0x8
	v_readfirstlane_b32 s3, v0
	s_ashr_i32 s12, s2, 5
	s_lshr_b32 s21, s3, 6
	s_and_b32 s3, s2, 7
	s_and_b32 s12, s12, -8
	s_load_dwordx8 s[4:11], s[0:1], 0x0
	s_or_b32 s12, s12, s3
	s_bfe_u32 s20, s2, 0x10003
	s_lshl_b32 s2, s2, 3
	s_and_b32 s2, s2, 0x780
	s_lshl_b32 s3, s21, 5
	s_ashr_i32 s13, s12, 31
	s_add_i32 s2, s3, s2
	s_lshl_b64 s[16:17], s[12:13], 11
	s_lshl_b32 s3, s20, 10
	s_or_b32 s14, s16, s3
	s_mov_b32 s15, s17
	s_lshl_b64 s[18:19], s[14:15], 7
	s_lshl_b64 s[14:15], s[12:13], 18
	s_waitcnt lgkmcnt(0)
	s_add_u32 s3, s8, s14
	s_addc_u32 s22, s9, s15
	s_add_u32 s16, s16, s2
	v_and_b32_e32 v98, 31, v0
	s_addc_u32 s17, s17, 0
	v_or_b32_e32 v2, s16, v98
	v_mov_b32_e32 v3, s17
	v_bfe_u32 v54, v0, 5, 1
	v_lshlrev_b64 v[2:3], 7, v[2:3]
	v_mov_b32_e32 v51, 0
	v_lshl_add_u64 v[2:3], s[4:5], 0, v[2:3]
	v_lshlrev_b32_e32 v50, 4, v54
	v_lshl_add_u64 v[2:3], v[2:3], 0, v[50:51]
	s_add_u32 s18, s6, s18
	v_bfe_u32 v1, v0, 3, 3
	global_load_dwordx4 v[94:97], v[2:3], off nt
	global_load_dwordx4 v[90:93], v[2:3], off offset:32 nt
	global_load_dwordx4 v[86:89], v[2:3], off offset:64 nt
	global_load_dwordx4 v[82:85], v[2:3], off offset:96 nt
	s_addc_u32 s19, s7, s19
	s_lshl_b32 s24, s20, 11
	v_lshl_or_b32 v2, s21, 4, v1
	v_and_b32_e32 v99, 63, v0
	s_add_u32 s4, s3, s24
	v_or_b32_e32 v3, 8, v2
	v_lshlrev_b32_e32 v4, 4, v0
	s_movk_i32 s3, 0x70
	v_bitop3_b32 v53, v99, s3, v4 bitop3:0x48
	v_lshrrev_b32_e32 v4, 1, v3
	v_xor_b32_e32 v4, v4, v0
	s_addc_u32 s5, s22, 0
	v_lshlrev_b32_e32 v4, 4, v4
	s_lshl_b32 s22, s21, 11
	v_and_b32_e32 v52, 0x70, v4
	v_lshl_or_b32 v55, v2, 7, v53
	s_mov_b32 m0, s22
	v_lshl_or_b32 v64, v3, 7, v52
	global_load_lds_dwordx4 v55, s[18:19]
	s_or_b32 m0, s22, 0x400
	v_lshl_or_b32 v50, v2, 12, v53
	global_load_lds_dwordx4 v64, s[18:19]
	s_add_i32 m0, s22, 0x2000
	v_lshl_or_b32 v2, v3, 12, v52
	global_load_lds_dwordx4 v50, s[4:5]
	s_add_i32 m0, s22, 0x2400
	v_mov_b32_e32 v3, v51
	global_load_lds_dwordx4 v2, s[4:5]
	s_add_i32 m0, s22, 0x4000
	v_lshl_add_u64 v[60:61], s[4:5], 0, v[50:51]
	v_lshl_add_u64 v[62:63], s[4:5], 0, v[2:3]
	s_add_u32 s4, s18, 0x2000
	s_addc_u32 s5, s19, 0
	s_add_i32 m0, s22, 0x4400
	s_load_dwordx2 s[0:1], s[0:1], 0x20
	s_mov_b64 s[4:5], 0x80
	v_lshl_add_u64 v[2:3], v[60:61], 0, s[4:5]
	s_add_i32 m0, s22, 0x6000
	v_lshrrev_b32_e32 v4, 1, v0
	v_lshl_add_u64 v[2:3], v[62:63], 0, s[4:5]
	s_add_i32 m0, s22, 0x6400
	v_and_b32_e32 v5, 4, v4
	v_lshlrev_b32_e32 v3, 1, v0
	v_and_b32_e32 v2, 19, v0
	v_and_b32_e32 v3, 8, v3
	v_or3_b32 v2, v3, v2, v5
	s_waitcnt vmcnt(0)
	v_lshlrev_b32_e32 v115, 7, v2
	v_lshrrev_b32_e32 v3, 1, v2
	v_bfe_u32 v46, v2, 1, 3
	v_bitop3_b32 v2, v54, v4, 7 bitop3:0x78
	s_mov_b32 s3, 0
	v_lshlrev_b32_e32 v108, 3, v54
	s_mov_b32 s23, 1
	s_mov_b64 s[16:17], 0x2000
	v_lshlrev_b32_e32 v109, 7, v98
	v_lshlrev_b32_e32 v110, 4, v2
	s_movk_i32 s25, 0x400
	v_bfe_u32 v50, v0, 1, 3
	s_barrier
	s_and_b32 s29, s28, 7
	s_lshr_b32 s40, s28, 3
	s_lshr_b32 s41, s40, 5
	s_lshl_b32 s41, s41, 3
	s_or_b32 s29, s41, s29
	s_and_b32 s40, s40, 1
	s_lshl_b32 s29, s29, 18
	s_lshl_b32 s41, s40, 17
	s_lshl_b32 s42, s40, 11
	s_add_i32 s41, s41, s29
	s_add_i32 s41, s41, 0x6000
	s_add_i32 s42, s42, s29
	s_add_i32 s42, s42, 0x180
	v_and_b32_e32 v145, 63, v0
	v_lshrrev_b32_e32 v146, 3, v145
	v_lshl_add_u32 v146, s21, 4, v146
	v_and_b32_e32 v145, 7, v145
	v_bfe_u32 v147, v146, 1, 3
	v_xor_b32_e32 v148, v145, v147
	v_xor_b32_e32 v147, 4, v148
	v_lshlrev_b32_e32 v148, 4, v148
	v_lshlrev_b32_e32 v147, 4, v147
	v_lshl_add_u32 v145, v146, 7, v148
	v_lshl_add_u32 v149, v146, 7, v147
	v_add_u32_e32 v149, 0x400, v149
	v_lshl_add_u32 v148, v146, 12, v148
	v_lshl_add_u32 v147, v146, 12, v147
	v_add_u32_e32 v147, 0x8000, v147
	s_waitcnt lgkmcnt(0)
	s_add_u32 s36, s32, s41
	s_addc_u32 s37, s33, 0
	s_add_u32 s38, s34, s42
	s_addc_u32 s39, s35, 0
	s_sub_u32 s40, s36, 0x4000
	s_subb_u32 s41, s37, 0
	s_sub_u32 s42, s38, 0x100
	s_subb_u32 s43, s39, 0
	s_add_i32 m0, s22, 0x4000
	s_nop 0
	global_load_lds_dwordx4 v145, s[40:41]
	s_add_i32 m0, s22, 0x4400
	s_nop 0
	global_load_lds_dwordx4 v149, s[40:41]
	s_add_i32 m0, s22, 0x6000
	s_nop 0
	global_load_lds_dwordx4 v148, s[42:43]
	s_add_i32 m0, s22, 0x6400
	s_nop 0
	global_load_lds_dwordx4 v147, s[42:43]
	v_bitop3_b32 v2, v54, v3, 7 bitop3:0x78
	v_lshlrev_b32_e32 v116, 4, v2
	v_bitop3_b32 v6, v54, v46, 2 bitop3:0x36
	v_lshlrev_b32_e32 v117, 4, v6
	v_bitop3_b32 v42, v54, v46, 4 bitop3:0x36
	v_bitop3_b32 v46, v54, v46, 6 bitop3:0x36
	v_lshlrev_b32_e32 v118, 4, v42
	v_lshlrev_b32_e32 v119, 4, v46
	v_bitop3_b32 v10, v54, v50, 2 bitop3:0x36
	v_lshlrev_b32_e32 v112, 4, v10
	v_bitop3_b32 v55, v54, v50, 4 bitop3:0x36
	v_bitop3_b32 v50, v54, v50, 6 bitop3:0x36
	v_lshlrev_b32_e32 v111, 4, v55
	v_lshlrev_b32_e32 v113, 4, v50
	v_mov_b32_e32 v2, 0
	v_mov_b32_e32 v3, 0
	v_mov_b32_e32 v4, 0
	v_mov_b32_e32 v5, 0
	v_mov_b32_e32 v6, 0
	v_mov_b32_e32 v7, 0
	v_mov_b32_e32 v8, 0
	v_mov_b32_e32 v9, 0
	v_mov_b32_e32 v10, 0
	v_mov_b32_e32 v11, 0
	v_mov_b32_e32 v12, 0
	v_mov_b32_e32 v13, 0
	v_mov_b32_e32 v14, 0
	v_mov_b32_e32 v15, 0
	v_mov_b32_e32 v16, 0
	v_mov_b32_e32 v17, 0
	v_mov_b32_e32 v18, 0
	v_mov_b32_e32 v19, 0
	v_mov_b32_e32 v20, 0
	v_mov_b32_e32 v21, 0
	v_mov_b32_e32 v22, 0
	v_mov_b32_e32 v23, 0
	v_mov_b32_e32 v24, 0
	v_mov_b32_e32 v25, 0
	v_mov_b32_e32 v26, 0
	v_mov_b32_e32 v27, 0
	v_mov_b32_e32 v28, 0
	v_mov_b32_e32 v29, 0
	v_mov_b32_e32 v30, 0
	v_mov_b32_e32 v31, 0
	v_mov_b32_e32 v32, 0
	v_mov_b32_e32 v33, 0
	v_mov_b32_e32 v34, 0
	v_mov_b32_e32 v35, 0
	v_mov_b32_e32 v36, 0
	v_mov_b32_e32 v37, 0
	v_mov_b32_e32 v38, 0
	v_mov_b32_e32 v39, 0
	v_mov_b32_e32 v40, 0
	v_mov_b32_e32 v41, 0
	v_mov_b32_e32 v42, 0
	v_mov_b32_e32 v43, 0
	v_mov_b32_e32 v44, 0
	v_mov_b32_e32 v45, 0
	v_mov_b32_e32 v46, 0
	v_mov_b32_e32 v47, 0
	v_mov_b32_e32 v48, 0
	v_mov_b32_e32 v49, 0
	v_mov_b32_e32 v114, 0
	s_mov_b32 s23, 0
	s_mov_b32 s9, 0
	s_mov_b32 s8, 0x46000000
	s_sub_u32 s36, s36, 0x2000
	s_subb_u32 s37, s37, 0
	s_sub_u32 s38, s38, 0x80
	s_subb_u32 s39, s39, 0
